# speedup vs baseline: 1.0119x; 1.0119x over previous
.LBB2_14:
	s_ashr_i32 s51, s50, 31
	s_lshl_b64 s[52:53], s[50:51], 10
	s_add_u32 s52, s10, s52
	s_addc_u32 s53, s11, s53
	v_mov_b32_e32 v162, v1
	s_barrier
	s_add_i32 s78, s70, 0x18000
	v_lshl_add_u64 v[2:3], s[52:53], 0, v[162:163]
	s_ashr_i32 s45, s44, 31
	v_lshl_add_u64 v[2:3], v[2:3], 0, s[20:21]
	s_mov_b32 m0, s78
	v_mov_b32_e32 v162, v1
	s_add_i32 s79, s70, 0x1a000
	s_lshl_b64 s[54:55], s[44:45], 10
	global_load_lds_dwordx4 v[2:3], off
	s_add_u32 s54, s8, s54
	v_lshl_add_u64 v[2:3], s[52:53], 0, v[162:163]
	v_lshl_add_u64 v[2:3], v[2:3], 0, s[22:23]
	s_mov_b32 m0, s79
	s_addc_u32 s55, s9, s55
	v_mov_b32_e32 v162, v1
	s_or_b32 s56, s50, 0x80
	global_load_lds_dwordx4 v[2:3], off
	s_add_i32 s45, s70, 0x8000
	v_lshl_add_u64 v[2:3], s[54:55], 0, v[162:163]
	s_ashr_i32 s57, s56, 31
	v_lshl_add_u64 v[2:3], v[2:3], 0, s[20:21]
	s_mov_b32 m0, s45
	v_mov_b32_e32 v162, v1
	s_add_i32 s80, s70, 0xa000
	s_lshl_b64 s[56:57], s[56:57], 10
	global_load_lds_dwordx4 v[2:3], off
	s_add_u32 s56, s10, s56
	v_lshl_add_u64 v[2:3], s[54:55], 0, v[162:163]
	v_lshl_add_u64 v[2:3], v[2:3], 0, s[22:23]
	s_mov_b32 m0, s80
	s_addc_u32 s57, s11, s57
	v_mov_b32_e32 v162, v1
	global_load_lds_dwordx4 v[2:3], off
	s_add_i32 s82, s70, 0x1c000
	v_lshl_add_u64 v[2:3], s[56:57], 0, v[162:163]
	v_lshl_add_u64 v[2:3], v[2:3], 0, s[20:21]
	s_mov_b32 m0, s82
	v_mov_b32_e32 v162, v1
	global_load_lds_dwordx4 v[2:3], off
	s_add_i32 s84, s70, 0x1e000
	v_lshl_add_u64 v[2:3], s[56:57], 0, v[162:163]
	v_lshl_add_u64 v[2:3], v[2:3], 0, s[22:23]
	s_mov_b32 m0, s84
	s_nop 0
	global_load_lds_dwordx4 v[2:3], off
	s_waitcnt lgkmcnt(0)
	s_cmp_lt_u32 s44, 0x800
	s_cbranch_scc1 .Lg2_bias_qk
	s_lshr_b32 s86, s44, 10
	s_cmp_eq_u32 s86, 1
	s_cselect_b32 s88, s14, s6
	s_cselect_b32 s89, s15, s7
	s_cmp_eq_u32 s86, 0
	s_cselect_b32 s88, s12, s88
	s_cselect_b32 s89, s13, s89
	s_and_b32 s86, s44, 0x3ff
	s_lshl_b32 s86, s86, 2
	s_add_u32 s88, s88, s86
	s_addc_u32 s89, s89, 0
	v_and_b32_e32 v184, 63, v0
	v_lshlrev_b32_e32 v184, 4, v184
	s_mov_b32 m0, 0x20000
	s_nop 0
	global_load_lds_dwordx4 v184, s[88:89]
	s_branch .Lg2_bias_done

.Lg2_wd:
	s_mov_b32 s85, -2
	s_mov_b64 s[56:57], 0
	s_barrier
	ds_read_b128 v[130:133], v164
	ds_read_b128 v[134:137], v164 offset:1024
	ds_read_b128 v[138:141], v164 offset:2048
	ds_read_b128 v[142:145], v164 offset:3072
	s_add_u32 s58, s54, s56
	v_mov_b32_e32 v162, v1
	s_addc_u32 s59, s55, s57
	ds_read_b128 v[146:149], v165
	ds_read_b128 v[150:153], v165 offset:1024
	ds_read_b128 v[154:157], v166
	ds_read_b128 v[158:161], v166 offset:1024
	ds_read_b128 v[172:175], v167
	ds_read_b128 v[176:179], v167 offset:1024
	ds_read_b128 v[180:183], v168
	ds_read_b128 v[184:187], v168 offset:1024
	s_add_i32 s81, s70, 0xc000
	v_lshl_add_u64 v[188:189], s[58:59], 0, v[162:163]
	v_lshl_add_u64 v[188:189], v[188:189], 0, s[24:25]
	s_mov_b32 m0, s81
	v_mov_b32_e32 v162, v1
	global_load_lds_dwordx4 v[188:189], off
	s_add_i32 s83, s70, 0xe000
	v_lshl_add_u64 v[188:189], s[58:59], 0, v[162:163]
	v_lshl_add_u64 v[188:189], v[188:189], 0, s[26:27]
	s_mov_b32 m0, s83
	s_nop 0
	global_load_lds_dwordx4 v[188:189], off
	s_waitcnt lgkmcnt(8)
	s_barrier
	s_waitcnt lgkmcnt(0)
	s_setprio 3
	s_waitcnt lgkmcnt(0)
	v_mfma_f32_16x16x128_f8f6f4 v[66:69], v[180:187], v[130:137], 0
	v_mfma_f32_16x16x128_f8f6f4 v[50:53], v[180:187], v[138:145], 0
	v_mfma_f32_16x16x128_f8f6f4 v[188:191], v[146:153], v[130:137], 0
	v_mfma_f32_16x16x128_f8f6f4 v[192:195], v[146:153], v[138:145], 0
	v_mfma_f32_16x16x128_f8f6f4 v[196:199], v[154:161], v[130:137], 0
	v_mfma_f32_16x16x128_f8f6f4 v[200:203], v[154:161], v[138:145], 0
	v_mfma_f32_16x16x128_f8f6f4 v[204:207], v[172:179], v[130:137], 0
	v_mfma_f32_16x16x128_f8f6f4 v[208:211], v[172:179], v[138:145], 0
	s_setprio 0
	s_barrier
	s_add_u32 s60, s52, s56
	v_mov_b32_e32 v162, v1
	s_addc_u32 s61, s53, s57
	s_nop 1
	ds_read_b128 v[82:85], v169
	ds_read_b128 v[86:89], v169 offset:1024
	ds_read_b128 v[122:125], v169 offset:2048
	ds_read_b128 v[126:129], v169 offset:3072
	s_add_i32 s77, s70, 0x10000
	v_lshl_add_u64 v[98:99], s[60:61], 0, v[162:163]
	v_lshl_add_u64 v[98:99], v[98:99], 0, s[28:29]
	s_mov_b32 m0, s77
	v_mov_b32_e32 v162, v1
	global_load_lds_dwordx4 v[98:99], off
	s_add_i32 s51, s70, 0x12000
	v_lshl_add_u64 v[98:99], s[60:61], 0, v[162:163]
	v_lshl_add_u64 v[98:99], v[98:99], 0, s[30:31]
	s_mov_b32 m0, s51
	s_nop 0
	global_load_lds_dwordx4 v[98:99], off
	s_barrier
	s_waitcnt lgkmcnt(0)
	s_setprio 3
	s_waitcnt lgkmcnt(0)
	v_mfma_f32_16x16x128_f8f6f4 v[118:121], v[146:153], v[82:89], 0
	v_mfma_f32_16x16x128_f8f6f4 v[114:117], v[146:153], v[122:129], 0
	v_mfma_f32_16x16x128_f8f6f4 v[212:215], v[154:161], v[82:89], 0
	v_mfma_f32_16x16x128_f8f6f4 v[154:157], v[154:161], v[122:129], 0
	v_mfma_f32_16x16x128_f8f6f4 v[158:161], v[172:179], v[82:89], 0
	v_mfma_f32_16x16x128_f8f6f4 v[172:175], v[172:179], v[122:129], 0
	v_mfma_f32_16x16x128_f8f6f4 v[176:179], v[180:187], v[82:89], 0
	v_mfma_f32_16x16x128_f8f6f4 v[180:183], v[180:187], v[122:129], 0
	s_setprio 0
	v_mov_b32_e32 v162, v1
	s_barrier
	s_nop 3
	ds_read_b128 v[74:77], v165 offset:16384
	ds_read_b128 v[78:81], v165 offset:17408
	ds_read_b128 v[90:93], v166 offset:16384
	ds_read_b128 v[94:97], v166 offset:17408
	ds_read_b128 v[98:101], v167 offset:16384
	ds_read_b128 v[102:105], v167 offset:17408
	ds_read_b128 v[106:109], v168 offset:16384
	ds_read_b128 v[110:113], v168 offset:17408
	s_mov_b32 m0, s70
	v_lshl_add_u64 v[146:147], s[58:59], 0, v[162:163]
	v_lshl_add_u64 v[146:147], v[146:147], 0, s[28:29]
	v_mov_b32_e32 v162, v1
	global_load_lds_dwordx4 v[146:147], off
	s_mov_b32 m0, s71
	v_lshl_add_u64 v[146:147], s[58:59], 0, v[162:163]
	v_lshl_add_u64 v[146:147], v[146:147], 0, s[30:31]
	global_load_lds_dwordx4 v[146:147], off
	s_barrier
	s_waitcnt lgkmcnt(0)
	s_setprio 3
	s_waitcnt lgkmcnt(0)
	v_mfma_f32_16x16x128_f8f6f4 v[62:65], v[74:81], v[130:137], 0
	v_mfma_f32_16x16x128_f8f6f4 v[54:57], v[74:81], v[138:145], 0
	v_mfma_f32_16x16x128_f8f6f4 v[42:45], v[90:97], v[130:137], 0
	v_mfma_f32_16x16x128_f8f6f4 v[216:219], v[90:97], v[138:145], 0
	v_mfma_f32_16x16x128_f8f6f4 v[220:223], v[98:105], v[130:137], 0
	v_mfma_f32_16x16x128_f8f6f4 v[224:227], v[98:105], v[138:145], 0
	v_mfma_f32_16x16x128_f8f6f4 v[228:231], v[106:113], v[130:137], 0
	v_mfma_f32_16x16x128_f8f6f4 v[232:235], v[106:113], v[138:145], 0
	s_setprio 0
	s_barrier
	v_mov_b32_e32 v162, v1
	s_add_i32 s75, s70, 0x14000
	s_nop 2
	v_lshl_add_u64 v[2:3], s[60:61], 0, v[162:163]
	v_lshl_add_u64 v[2:3], v[2:3], 0, s[34:35]
	s_mov_b32 m0, s75
	v_mov_b32_e32 v162, v1
	global_load_lds_dwordx4 v[2:3], off
	s_add_i32 s76, s70, 0x16000
	v_lshl_add_u64 v[2:3], s[60:61], 0, v[162:163]
	v_lshl_add_u64 v[2:3], v[2:3], 0, s[36:37]
	s_mov_b32 m0, s76
	s_nop 0
	global_load_lds_dwordx4 v[2:3], off
	s_waitcnt vmcnt(6)
	s_barrier
	s_setprio 3
	v_mfma_f32_16x16x128_f8f6f4 v[70:73], v[74:81], v[82:89], 0
	v_mfma_f32_16x16x128_f8f6f4 v[58:61], v[74:81], v[122:129], 0
	v_mfma_f32_16x16x128_f8f6f4 v[46:49], v[90:97], v[82:89], 0
	v_mfma_f32_16x16x128_f8f6f4 v[236:239], v[90:97], v[122:129], 0
	v_mfma_f32_16x16x128_f8f6f4 v[240:243], v[98:105], v[82:89], 0
	v_mfma_f32_16x16x128_f8f6f4 v[244:247], v[98:105], v[122:129], 0
	v_mfma_f32_16x16x128_f8f6f4 v[248:251], v[106:113], v[82:89], 0
	v_mfma_f32_16x16x128_f8f6f4 v[252:255], v[106:113], v[122:129], 0
	s_setprio 0
	s_barrier
	ds_read_b128 v[2:5], v170
	s_nop 3
	ds_read_b128 v[6:9], v170 offset:1024
	ds_read_b128 v[130:133], v170 offset:2048
	ds_read_b128 v[134:137], v170 offset:3072
	v_mov_b32_e32 v162, v1
	ds_read_b128 v[10:13], v165 offset:32768
	ds_read_b128 v[14:17], v165 offset:33792
	ds_read_b128 v[18:21], v166 offset:32768
	ds_read_b128 v[22:25], v166 offset:33792
	ds_read_b128 v[26:29], v167 offset:32768
	ds_read_b128 v[30:33], v167 offset:33792
	ds_read_b128 v[34:37], v168 offset:32768
	ds_read_b128 v[38:41], v168 offset:33792
	s_mov_b32 m0, s72
	v_lshl_add_u64 v[74:75], s[58:59], 0, v[162:163]
	v_lshl_add_u64 v[74:75], v[74:75], 0, s[34:35]
	v_mov_b32_e32 v162, v1
	global_load_lds_dwordx4 v[74:75], off
	s_mov_b32 m0, s73
	v_lshl_add_u64 v[74:75], s[58:59], 0, v[162:163]
	v_lshl_add_u64 v[74:75], v[74:75], 0, s[36:37]
	global_load_lds_dwordx4 v[74:75], off
	s_waitcnt lgkmcnt(8)
	s_barrier
	s_waitcnt lgkmcnt(0)
	s_setprio 3
	s_waitcnt lgkmcnt(0)
	v_mfma_f32_16x16x128_f8f6f4 v[126:129], v[10:17], v[2:9], v[188:191]
	v_mfma_f32_16x16x128_f8f6f4 v[122:125], v[10:17], v[130:137], v[192:195]
	v_mfma_f32_16x16x128_f8f6f4 v[110:113], v[18:25], v[2:9], v[196:199]
	v_mfma_f32_16x16x128_f8f6f4 v[98:101], v[18:25], v[130:137], v[200:203]
	v_mfma_f32_16x16x128_f8f6f4 v[86:89], v[26:33], v[2:9], v[204:207]
	v_mfma_f32_16x16x128_f8f6f4 v[82:85], v[26:33], v[130:137], v[208:211]
	v_mfma_f32_16x16x128_f8f6f4 v[66:69], v[34:41], v[2:9], v[66:69]
	v_mfma_f32_16x16x128_f8f6f4 v[50:53], v[34:41], v[130:137], v[50:53]
	s_setprio 0
	s_barrier
	v_mov_b32_e32 v162, v1
	ds_read_b128 v[138:141], v171
	ds_read_b128 v[142:145], v171 offset:1024
	ds_read_b128 v[146:149], v171 offset:2048
	ds_read_b128 v[150:153], v171 offset:3072
	s_mov_b32 m0, s78
	v_lshl_add_u64 v[74:75], s[60:61], 0, v[162:163]
	v_lshl_add_u64 v[74:75], v[74:75], 0, s[38:39]
	v_mov_b32_e32 v162, v1
	global_load_lds_dwordx4 v[74:75], off
	s_mov_b32 m0, s79
	v_lshl_add_u64 v[74:75], s[60:61], 0, v[162:163]
	v_lshl_add_u64 v[74:75], v[74:75], 0, s[40:41]
	global_load_lds_dwordx4 v[74:75], off
	s_barrier
	s_waitcnt lgkmcnt(0)
	s_setprio 3
	s_waitcnt lgkmcnt(0)
	v_mfma_f32_16x16x128_f8f6f4 v[118:121], v[10:17], v[138:145], v[118:121]
	v_mfma_f32_16x16x128_f8f6f4 v[114:117], v[10:17], v[146:153], v[114:117]
	v_mfma_f32_16x16x128_f8f6f4 v[106:109], v[18:25], v[138:145], v[212:215]
	v_mfma_f32_16x16x128_f8f6f4 v[102:105], v[18:25], v[146:153], v[154:157]
	v_mfma_f32_16x16x128_f8f6f4 v[94:97], v[26:33], v[138:145], v[158:161]
	v_mfma_f32_16x16x128_f8f6f4 v[90:93], v[26:33], v[146:153], v[172:175]
	v_mfma_f32_16x16x128_f8f6f4 v[78:81], v[34:41], v[138:145], v[176:179]
	v_mfma_f32_16x16x128_f8f6f4 v[74:77], v[34:41], v[146:153], v[180:183]
	s_setprio 0
	v_mov_b32_e32 v162, v1
	s_barrier
	ds_read_b128 v[154:157], v165 offset:49152
	ds_read_b128 v[158:161], v165 offset:50176
	ds_read_b128 v[172:175], v166 offset:49152
	ds_read_b128 v[176:179], v166 offset:50176
	ds_read_b128 v[180:183], v167 offset:49152
	ds_read_b128 v[184:187], v167 offset:50176
	ds_read_b128 v[188:191], v168 offset:49152
	ds_read_b128 v[192:195], v168 offset:50176
	s_mov_b32 m0, s45
	v_lshl_add_u64 v[10:11], s[58:59], 0, v[162:163]
	v_lshl_add_u64 v[10:11], v[10:11], 0, s[38:39]
	v_mov_b32_e32 v162, v1
	global_load_lds_dwordx4 v[10:11], off
	s_mov_b32 m0, s80
	v_lshl_add_u64 v[10:11], s[58:59], 0, v[162:163]
	v_lshl_add_u64 v[10:11], v[10:11], 0, s[40:41]
	global_load_lds_dwordx4 v[10:11], off
	s_barrier
	s_waitcnt lgkmcnt(0)
	s_setprio 3
	s_waitcnt lgkmcnt(0)
	v_mfma_f32_16x16x128_f8f6f4 v[62:65], v[154:161], v[2:9], v[62:65]
	v_mfma_f32_16x16x128_f8f6f4 v[54:57], v[154:161], v[130:137], v[54:57]
	v_mfma_f32_16x16x128_f8f6f4 v[42:45], v[172:179], v[2:9], v[42:45]
	v_mfma_f32_16x16x128_f8f6f4 v[34:37], v[172:179], v[130:137], v[216:219]
	v_mfma_f32_16x16x128_f8f6f4 v[26:29], v[180:187], v[2:9], v[220:223]
	v_mfma_f32_16x16x128_f8f6f4 v[18:21], v[180:187], v[130:137], v[224:227]
	v_mfma_f32_16x16x128_f8f6f4 v[10:13], v[188:195], v[2:9], v[228:231]
	v_mfma_f32_16x16x128_f8f6f4 v[2:5], v[188:195], v[130:137], v[232:235]
	s_setprio 0
	s_barrier
	v_mov_b32_e32 v162, v1
	s_mov_b32 m0, s82
	v_lshl_add_u64 v[6:7], s[60:61], 0, v[162:163]
	v_lshl_add_u64 v[6:7], v[6:7], 0, s[42:43]
	v_mov_b32_e32 v162, v1
	global_load_lds_dwordx4 v[6:7], off
	s_mov_b32 m0, s84
	v_lshl_add_u64 v[6:7], s[60:61], 0, v[162:163]
	v_lshl_add_u64 v[6:7], v[6:7], 0, s[46:47]
	global_load_lds_dwordx4 v[6:7], off
	s_waitcnt vmcnt(6)
	s_barrier
	s_setprio 3
	v_mfma_f32_16x16x128_f8f6f4 v[70:73], v[154:161], v[138:145], v[70:73]
	v_mfma_f32_16x16x128_f8f6f4 v[58:61], v[154:161], v[146:153], v[58:61]
	v_mfma_f32_16x16x128_f8f6f4 v[46:49], v[172:179], v[138:145], v[46:49]
	v_mfma_f32_16x16x128_f8f6f4 v[38:41], v[172:179], v[146:153], v[236:239]
	v_mfma_f32_16x16x128_f8f6f4 v[30:33], v[180:187], v[138:145], v[240:243]
	v_mfma_f32_16x16x128_f8f6f4 v[22:25], v[180:187], v[146:153], v[244:247]
	v_mfma_f32_16x16x128_f8f6f4 v[14:17], v[188:195], v[138:145], v[248:251]
	v_mfma_f32_16x16x128_f8f6f4 v[6:9], v[188:195], v[146:153], v[252:255]
	s_setprio 0
	s_add_i32 s85, s85, 2
	s_add_u32 s56, s56, 0x100
	s_addc_u32 s57, s57, 0
	s_cmp_lt_u32 s85, 4
	s_barrier

.LBB2_26:
	s_endpgm
	s_nop 0
	s_nop 0
	s_nop 0
	s_nop 0
	s_nop 0
	s_nop 0
	s_nop 0
	s_nop 0
	s_nop 0
	s_nop 0
	s_nop 0
	s_nop 0
	s_nop 0
	s_nop 0
	s_nop 0
	s_nop 0
	s_nop 0
	s_nop 0
	s_nop 0
	s_nop 0
	s_nop 0
	s_nop 0
	s_nop 0
	s_nop 0
	s_nop 0
	s_endpgm
